# k_iter: one-wave section between barriers shortened (readlane for ref, A*rcp(ref) before the f16 rounding, DPP neighbour)
# speedup vs baseline: 1.0475x; 1.0023x over previous
.LBB2_94:
	s_or_b64 exec, exec, s[22:23]
	s_waitcnt lgkmcnt(0)
	s_barrier
	s_and_saveexec_b64 s[22:23], s[8:9]
	s_cbranch_execz .LBB2_99
	ds_read_b32 v4, v46 offset:29728
	v_add_u32_e32 v10, 32, v46
	ds_read2st64_b32 v[2:3], v10 offset0:108 offset1:109
	ds_read2st64_b32 v[6:7], v10 offset0:110 offset1:111
	ds_read2st64_b32 v[8:9], v10 offset0:112 offset1:113
	ds_read2st64_b32 v[10:11], v10 offset0:114 offset1:115
	s_waitcnt lgkmcnt(3)
	v_add_f32_e32 v2, v4, v2
	v_add_f32_e32 v2, v2, v3
	s_waitcnt lgkmcnt(2)
	v_add_f32_e32 v2, v2, v6
	v_add_f32_e32 v2, v2, v7
	s_waitcnt lgkmcnt(1)
	v_add_f32_e32 v2, v2, v8
	v_add_f32_e32 v2, v2, v9
	s_waitcnt lgkmcnt(0)
	v_add_f32_e32 v2, v2, v10
	v_add_f32_e32 v2, v2, v11
	v_rcp_f32_e32 v3, v2
	v_cmp_lt_f32_e32 vcc, 0, v2
	v_mbcnt_lo_u32_b32 v4, -1, 0
	v_mbcnt_hi_u32_b32 v4, -1, v4
	v_cndmask_b32_e32 v6, 0, v3, vcc
	v_cmp_lt_f32_e32 vcc, 0, v6
	s_ff1_i32_b64 s8, vcc
	s_cmp_lg_u64 vcc, 0
	s_cselect_b32 s8, s8, 0
	ds_write_b32 v46, v6 offset:29984
	s_nop 0
	v_readlane_b32 s9, v6, s8
	s_nop 3
	v_mov_b32_e32 v2, s9
	v_cmp_lt_f32_e32 vcc, 0, v2
	s_nop 1
	v_cndmask_b32_e32 v2, 1.0, v2, vcc
	v_rcp_f32_e32 v4, v2
	s_nop 0
	v_mul_f32_e32 v3, v6, v4
	v_min_f32_e32 v3, 0x476a6000, v3
	s_nop 1
	v_mov_b32_dpp v4, v3 row_shl:1 row_mask:0xf bank_mask:0xf
	v_cmp_eq_u32_e32 vcc, 0, v5
	s_and_saveexec_b64 s[8:9], vcc
	s_cbranch_execz .LBB2_97
	v_lshlrev_b32_e32 v0, 1, v0
	s_waitcnt lgkmcnt(0)
	v_cvt_pk_f16_f32 v3, v3, v4
	ds_write_b32 v0, v3 offset:30240

.LBB3_107:
	s_or_b64 exec, exec, s[6:7]
	s_waitcnt lgkmcnt(0)
	s_barrier
	s_and_saveexec_b64 s[6:7], s[14:15]
	s_cbranch_execz .LBB3_112
	ds_read_b32 v10, v1 offset:5152
	v_add_u32_e32 v8, 32, v1
	ds_read2st64_b32 v[2:3], v8 offset0:12 offset1:13
	ds_read2st64_b32 v[4:5], v8 offset0:14 offset1:15
	ds_read2st64_b32 v[6:7], v8 offset0:16 offset1:17
	ds_read2st64_b32 v[8:9], v8 offset0:18 offset1:19
	s_waitcnt lgkmcnt(3)
	v_add_f32_e32 v2, v10, v2
	v_add_f32_e32 v2, v2, v3
	s_waitcnt lgkmcnt(2)
	v_add_f32_e32 v2, v2, v4
	v_add_f32_e32 v2, v2, v5
	s_waitcnt lgkmcnt(1)
	v_add_f32_e32 v2, v2, v6
	v_add_f32_e32 v2, v2, v7
	s_waitcnt lgkmcnt(0)
	v_add_f32_e32 v2, v2, v8
	v_add_f32_e32 v2, v2, v9
	v_rcp_f32_e32 v3, v2
	v_cmp_lt_f32_e32 vcc, 0, v2
	v_mbcnt_lo_u32_b32 v4, -1, 0
	v_mbcnt_hi_u32_b32 v4, -1, v4
	v_cndmask_b32_e32 v5, 0, v3, vcc
	v_cmp_lt_f32_e32 vcc, 0, v5
	s_ff1_i32_b64 s8, vcc
	s_cmp_lg_u64 vcc, 0
	s_cselect_b32 s8, s8, 0
	ds_write_b32 v1, v5 offset:5408
	s_nop 0
	v_readlane_b32 s9, v5, s8
	s_nop 3
	v_mov_b32_e32 v2, s9
	v_cmp_lt_f32_e32 vcc, 0, v2
	s_nop 1
	v_cndmask_b32_e32 v2, 1.0, v2, vcc
	v_rcp_f32_e32 v4, v2
	s_nop 0
	v_mul_f32_e32 v3, v5, v4
	v_min_f32_e32 v3, 0x476a6000, v3
	s_nop 1
	v_mov_b32_dpp v4, v3 row_shl:1 row_mask:0xf bank_mask:0xf
	v_cmp_eq_u32_e32 vcc, 0, v38
	s_and_saveexec_b64 s[8:9], vcc
	s_cbranch_execz .LBB3_110
	v_lshlrev_b32_e32 v1, 1, v0
	s_waitcnt lgkmcnt(0)
	v_cvt_pk_f16_f32 v3, v3, v4
	ds_write_b32 v1, v3 offset:5664

.LBB4_39:
	s_waitcnt vmcnt(5)
	v_rcp_f32_e32 v2, v133
	s_waitcnt vmcnt(4)
	v_rcp_f32_e32 v3, v132
	s_waitcnt vmcnt(3)
	v_rcp_f32_e32 v4, v131
	v_cmp_lt_f32_e32 vcc, 0, v133
	s_waitcnt vmcnt(2)
	v_rcp_f32_e32 v5, v130
	s_waitcnt vmcnt(1)
	v_rcp_f32_e32 v6, v129
	v_cndmask_b32_e32 v2, 0, v2, vcc
	v_cmp_lt_f32_e32 vcc, 0, v132
	s_waitcnt vmcnt(0)
	v_rcp_f32_e32 v7, v128
	s_getpc_b64 s[36:37]
	s_sub_u32 s36, s36, 0x902c
	s_subb_u32 s37, s37, 0
	v_lshlrev_b32_e32 v183, 6, v0
	v_min_u32_e32 v183, 0x1980, v183
	global_load_dword v183, v183, s[36:37]
	s_mov_b32 s4, 0x42c80000
	v_cndmask_b32_e32 v3, 0, v3, vcc
	v_cmp_lt_f32_e32 vcc, 0, v131
	v_cmp_ngt_f32_e64 s[2:3], s4, v3
	s_mov_b64 s[6:7], 0
	v_cndmask_b32_e32 v4, 0, v4, vcc
	v_cmp_lt_f32_e32 vcc, 0, v130
	s_nop 1
	v_cndmask_b32_e32 v5, 0, v5, vcc
	v_cmp_lt_f32_e32 vcc, 0, v129
	s_nop 1
	v_cndmask_b32_e32 v6, 0, v6, vcc
	v_cmp_lt_f32_e32 vcc, 0, v128
	s_nop 1
	v_cndmask_b32_e32 v7, 0, v7, vcc
	v_cmp_ngt_f32_e32 vcc, s4, v2
	s_or_b64 s[2:3], vcc, s[2:3]
	v_cmp_ngt_f32_e32 vcc, s4, v4
	s_or_b64 s[2:3], s[2:3], vcc
	v_cmp_ngt_f32_e32 vcc, s4, v5
	s_or_b64 s[2:3], s[2:3], vcc
	v_cmp_ngt_f32_e32 vcc, s4, v6
	s_or_b64 s[2:3], s[2:3], vcc
	v_cmp_ngt_f32_e32 vcc, s4, v7
	s_or_b64 s[2:3], s[2:3], vcc
	v_cndmask_b32_e64 v8, 0, 1, s[2:3]
	v_cmp_ne_u32_e32 vcc, 0, v8
	s_cmp_eq_u64 vcc, 0
	s_cselect_b64 s[2:3], -1, 0
	v_cndmask_b32_e64 v8, 0, 1, s[2:3]
	s_nop 0
	v_readfirstlane_b32 s2, v8
	s_bitcmp0_b32 s2, 0
	s_cbranch_scc0 .LBB4_45
	s_cmp_lt_i32 s28, 4
	s_cbranch_scc1 .LBB4_46
	s_cmp_gt_i32 s28, 4
	s_cbranch_scc0 .LBB4_47
	s_mov_b64 s[4:5], -1
	v_mov_b32_e32 v8, 0
	s_cmp_gt_i32 s28, 5
	v_mov_b32_e32 v167, 0
	v_mov_b32_e32 v166, 0
	v_mov_b32_e32 v165, 0
	v_mov_b32_e32 v164, 0
	v_mov_b32_e32 v162, 0
	v_mov_b32_e32 v160, 0
	v_mov_b32_e32 v159, 0
	v_mov_b32_e32 v157, 0
	v_mov_b32_e32 v151, 0
	v_mov_b32_e32 v149, 0
	v_mov_b32_e32 v147, 0
	v_mov_b32_e32 v146, 0
	v_mov_b32_e32 v144, 0
	v_mov_b32_e32 v143, 0
	v_mov_b32_e32 v152, 0
	v_mov_b32_e32 v153, 0
	v_mov_b32_e32 v154, 0
	v_mov_b32_e32 v155, 0
	v_mov_b32_e32 v156, 0
	v_mov_b32_e32 v158, 0
	v_mov_b32_e32 v161, 0
	v_mov_b32_e32 v163, 0
	v_mov_b32_e32 v168, 0
	v_mov_b32_e32 v169, 0
	v_mov_b32_e32 v170, 0
	v_mov_b32_e32 v171, 0
	v_mov_b32_e32 v172, 0
	v_mov_b32_e32 v173, 0
	v_mov_b32_e32 v174, 0
	v_mov_b32_e32 v145, 0
	v_mov_b32_e32 v148, 0
	v_mov_b32_e32 v150, 0
	s_cbranch_scc0 .LBB4_50
	s_cmp_eq_u32 s28, 6
	s_cbranch_scc0 .LBB4_49
	v_mov_b32_e32 v145, 0
	v_mov_b32_e32 v148, 0
	v_mov_b32_e32 v150, 0
	v_mov_b32_e32 v143, 0
	v_mov_b32_e32 v144, 0
	v_mov_b32_e32 v146, 0
	v_mov_b32_e32 v147, 0
	v_mov_b32_e32 v149, 0
	v_mov_b32_e32 v151, 0
	v_mov_b32_e32 v152, 0
	v_mov_b32_e32 v153, 0
	v_mov_b32_e32 v154, 0
	v_mov_b32_e32 v155, 0
	v_mov_b32_e32 v156, 0
	v_mov_b32_e32 v158, 0
	v_mov_b32_e32 v161, 0
	v_mov_b32_e32 v163, 0
	v_mov_b32_e32 v157, 0
	v_mov_b32_e32 v159, 0
	v_mov_b32_e32 v160, 0
	v_mov_b32_e32 v162, 0
	v_mov_b32_e32 v164, 0
	v_mov_b32_e32 v165, 0
	v_mov_b32_e32 v166, 0
	v_mov_b32_e32 v167, 0
	v_mov_b32_e32 v168, 0
	v_mov_b32_e32 v169, 0
	v_mov_b32_e32 v170, 0
	v_mov_b32_e32 v171, 0
	v_mov_b32_e32 v172, 0
	v_mov_b32_e32 v173, 0
	v_mov_b32_e32 v174, 0
	v_fma_mix_f32 v148, v43, v7, v148 op_sel_hi:[1,0,0]
	v_fma_mix_f32 v150, v45, v7, v150 op_sel_hi:[1,0,0]
	v_fma_mix_f32 v143, v50, v7, v143 op_sel_hi:[1,0,0]
	v_fma_mix_f32 v144, v54, v7, v144 op_sel_hi:[1,0,0]
	v_fma_mix_f32 v146, v58, v7, v146 op_sel_hi:[1,0,0]
	v_fma_mix_f32 v147, v61, v7, v147 op_sel_hi:[1,0,0]
	v_fma_mix_f32 v149, v64, v7, v149 op_sel_hi:[1,0,0]
	v_fma_mix_f32 v151, v66, v7, v151 op_sel_hi:[1,0,0]
	v_fma_mix_f32 v152, v43, v7, v152 op_sel:[1,0,0] op_sel_hi:[1,0,0]
	v_fma_mix_f32 v153, v45, v7, v153 op_sel:[1,0,0] op_sel_hi:[1,0,0]
	v_fma_mix_f32 v154, v50, v7, v154 op_sel:[1,0,0] op_sel_hi:[1,0,0]
	v_fma_mix_f32 v155, v54, v7, v155 op_sel:[1,0,0] op_sel_hi:[1,0,0]
	v_fma_mix_f32 v156, v58, v7, v156 op_sel:[1,0,0] op_sel_hi:[1,0,0]
	v_fma_mix_f32 v158, v61, v7, v158 op_sel:[1,0,0] op_sel_hi:[1,0,0]
	v_fma_mix_f32 v161, v64, v7, v161 op_sel:[1,0,0] op_sel_hi:[1,0,0]
	v_fma_mix_f32 v163, v66, v7, v163 op_sel:[1,0,0] op_sel_hi:[1,0,0]
	v_fma_mix_f32 v157, v72, v7, v157 op_sel_hi:[1,0,0]
	v_fma_mix_f32 v159, v76, v7, v159 op_sel_hi:[1,0,0]
	v_fma_mix_f32 v160, v83, v7, v160 op_sel_hi:[1,0,0]
	v_fma_mix_f32 v162, v85, v7, v162 op_sel_hi:[1,0,0]
	v_fma_mix_f32 v164, v89, v7, v164 op_sel_hi:[1,0,0]
	v_fma_mix_f32 v165, v92, v7, v165 op_sel_hi:[1,0,0]
	v_fma_mix_f32 v166, v95, v7, v166 op_sel_hi:[1,0,0]
	v_fma_mix_f32 v167, v96, v7, v167 op_sel_hi:[1,0,0]
	v_fma_mix_f32 v168, v72, v7, v168 op_sel:[1,0,0] op_sel_hi:[1,0,0]
	v_fma_mix_f32 v169, v76, v7, v169 op_sel:[1,0,0] op_sel_hi:[1,0,0]
	v_fma_mix_f32 v170, v83, v7, v170 op_sel:[1,0,0] op_sel_hi:[1,0,0]
	v_fma_mix_f32 v171, v85, v7, v171 op_sel:[1,0,0] op_sel_hi:[1,0,0]
	v_fma_mix_f32 v172, v89, v7, v172 op_sel:[1,0,0] op_sel_hi:[1,0,0]
	v_fma_mix_f32 v173, v92, v7, v173 op_sel:[1,0,0] op_sel_hi:[1,0,0]
	v_fma_mix_f32 v174, v95, v7, v174 op_sel:[1,0,0] op_sel_hi:[1,0,0]
	v_fma_mix_f32 v145, v96, v7, v145 op_sel:[1,0,0] op_sel_hi:[1,0,0]
	s_branch .LBB4_50

.LBB4_107:
	s_or_b64 exec, exec, s[6:7]
	s_waitcnt lgkmcnt(0)
	s_barrier
	s_and_saveexec_b64 s[6:7], s[14:15]
	s_cbranch_execz .LBB4_113
	ds_read_b32 v10, v1 offset:5152
	v_add_u32_e32 v8, 32, v1
	ds_read2st64_b32 v[2:3], v8 offset0:12 offset1:13
	ds_read2st64_b32 v[4:5], v8 offset0:14 offset1:15
	ds_read2st64_b32 v[6:7], v8 offset0:16 offset1:17
	ds_read2st64_b32 v[8:9], v8 offset0:18 offset1:19
	s_waitcnt lgkmcnt(3)
	v_add_f32_e32 v2, v10, v2
	v_add_f32_e32 v2, v2, v3
	s_waitcnt lgkmcnt(2)
	v_add_f32_e32 v2, v2, v4
	v_add_f32_e32 v2, v2, v5
	s_waitcnt lgkmcnt(1)
	v_add_f32_e32 v2, v2, v6
	v_add_f32_e32 v2, v2, v7
	s_waitcnt lgkmcnt(0)
	v_add_f32_e32 v2, v2, v8
	v_add_f32_e32 v2, v2, v9
	v_rcp_f32_e32 v3, v2
	v_cmp_lt_f32_e32 vcc, 0, v2
	v_mbcnt_lo_u32_b32 v4, -1, 0
	v_mbcnt_hi_u32_b32 v5, -1, v4
	v_cndmask_b32_e32 v2, 0, v3, vcc
	v_cmp_lt_f32_e32 vcc, 0, v2
	s_ff1_i32_b64 s8, vcc
	s_cmp_lg_u64 vcc, 0
	s_cselect_b32 s8, s8, 0
	ds_write_b32 v1, v2 offset:5408
	s_nop 0
	v_readlane_b32 s9, v2, s8
	s_nop 3
	v_mov_b32_e32 v3, s9
	v_cmp_lt_f32_e32 vcc, 0, v3
	s_nop 1
	v_cndmask_b32_e32 v3, 1.0, v3, vcc
	v_rcp_f32_e32 v5, v3
	s_nop 0
	v_mul_f32_e32 v4, v2, v5
	v_min_f32_e32 v4, 0x476a6000, v4
	s_nop 1
	v_mov_b32_dpp v5, v4 row_shl:1 row_mask:0xf bank_mask:0xf
	v_cmp_eq_u32_e32 vcc, 0, v38
	s_and_saveexec_b64 s[8:9], vcc
	s_cbranch_execz .LBB4_110
	v_lshlrev_b32_e32 v1, 1, v0
	s_waitcnt lgkmcnt(0)
	v_cvt_pk_f16_f32 v4, v4, v5
	ds_write_b32 v1, v4 offset:5664
